# combination of the individually neutral trims: packed side-stream consume (GEMM1), adaLN remainder loop unrolled, GEMM2 loop-invariant LDS read addresses
# baseline (speedup 1.0000x reference)
.LBB0_1008:
	s_add_u32 s5, s38, 0x100
	s_addc_u32 s27, s39, 0
	s_lshl_b32 s44, s61, 8
	s_lshl_b32 s29, s61, 19
	s_bitset1_b32 s44, 7
	s_mov_b32 s45, -2
	s_mov_b64 s[38:39], 0
	s_cmp_eq_u32 s45, 12
	s_cselect_b64 s[42:43], -1, 0
	s_and_b64 s[40:41], s[36:37], s[42:43]
	s_andn2_b64 vcc, exec, s[40:41]
	v_mov_b32_e32 v131, v138
	v_mov_b32_e32 v133, v128
	s_add_u32 s64, s6, s38
	ds_read_b128 v[178:181], v164
	ds_read_b128 v[186:189], v164 offset:2048
	ds_read_b128 v[182:185], v165
	ds_read_b128 v[190:193], v165 offset:2048
	s_addc_u32 s65, s7, s39
	ds_read_b128 v[194:197], v166
	ds_read_b128 v[202:205], v166 offset:2048
	ds_read_b128 v[198:201], v167
	ds_read_b128 v[206:209], v167 offset:2048
	s_add_u32 s66, s64, 0x5e000100
	s_addc_u32 s67, s65, 0
	s_and_b64 s[40:41], s[42:43], exec
	s_cselect_b32 s41, s11, s67
	s_cselect_b32 s40, s10, s66
	s_add_u32 s66, s5, s38
	s_addc_u32 s67, s27, s39
	s_and_b64 s[42:43], s[42:43], exec
	s_cselect_b32 s43, s35, s67
	s_cselect_b32 s42, s34, s66
	ds_read_b128 v[210:213], v175
	ds_read_b128 v[218:221], v175 offset:2048
	ds_read_b128 v[214:217], v176
	ds_read_b128 v[222:225], v176 offset:2048
	ds_read_b128 v[226:229], v175 offset:4096
	ds_read_b128 v[234:237], v175 offset:6144
	ds_read_b128 v[230:233], v176 offset:4096
	ds_read_b128 v[238:241], v176 offset:6144
	s_add_i32 m0, s1, 0xc000
	s_add_u32 vcc_lo, s64, s16
	s_addc_u32 vcc_hi, s65, s17
	global_load_lds_dwordx4 v128, vcc
	v_mov_b32_e32 v139, v129
	s_add_i32 m0, s1, 0xe000
	s_nop 0
	global_load_lds_dwordx4 v138, vcc
	s_waitcnt vmcnt(8)
	s_waitcnt lgkmcnt(0)
	s_barrier
	s_setprio 1
	s_waitcnt lgkmcnt(0)
	v_mfma_f32_16x16x128_f8f6f4 v[100:103], v[178:185], v[210:217], 0
	v_mfma_f32_16x16x128_f8f6f4 v[96:99], v[186:193], v[210:217], 0
	v_mfma_f32_16x16x128_f8f6f4 v[92:95], v[178:185], v[218:225], 0
	v_mfma_f32_16x16x128_f8f6f4 v[88:91], v[186:193], v[218:225], 0
	v_mfma_f32_16x16x128_f8f6f4 v[84:87], v[178:185], v[226:233], 0
	v_mfma_f32_16x16x128_f8f6f4 v[80:83], v[186:193], v[226:233], 0
	v_mfma_f32_16x16x128_f8f6f4 v[242:245], v[178:185], v[234:241], 0
	v_mfma_f32_16x16x128_f8f6f4 v[246:249], v[186:193], v[234:241], 0
	s_setprio 0
	s_setprio 1
	v_mfma_f32_16x16x128_f8f6f4 v[40:43], v[194:201], v[234:241], 0
	v_mfma_f32_16x16x128_f8f6f4 v[32:35], v[202:209], v[234:241], 0
	v_mfma_f32_16x16x128_f8f6f4 v[250:253], v[194:201], v[210:217], 0
	v_mfma_f32_16x16x128_f8f6f4 v[144:147], v[202:209], v[210:217], 0
	v_mfma_f32_16x16x128_f8f6f4 v[148:151], v[194:201], v[218:225], 0
	v_mfma_f32_16x16x128_f8f6f4 v[152:155], v[202:209], v[218:225], 0
	v_mfma_f32_16x16x128_f8f6f4 v[156:159], v[194:201], v[226:233], 0
	v_mfma_f32_16x16x128_f8f6f4 v[160:163], v[202:209], v[226:233], 0
	s_setprio 0
	s_barrier
	s_add_i32 s64, s58, s48
	s_mov_b32 m0, s64
	s_nop 2
	s_nop 0
	global_load_lds_dwordx4 v136, s[42:43]
	s_add_i32 m0, s64, 0x2000
	s_add_u32 s64, s42, 0x4000
	s_addc_u32 s65, s43, 0
	s_add_i32 s66, s59, s48
	s_nop 0
	global_load_lds_dwordx4 v130, s[42:43]
	s_mov_b32 m0, s66
	s_nop 0
	global_load_lds_dwordx4 v136, s[64:65]
	s_add_i32 m0, s66, 0x2000
	s_nop 0
	global_load_lds_dwordx4 v130, s[64:65]
	ds_read_b128 v[48:51], v175 offset:16384
	ds_read_b128 v[56:59], v175 offset:18432
	ds_read_b128 v[52:55], v176 offset:16384
	ds_read_b128 v[60:63], v176 offset:18432
	ds_read_b128 v[64:67], v175 offset:20480
	ds_read_b128 v[72:75], v175 offset:22528
	ds_read_b128 v[68:71], v176 offset:20480
	ds_read_b128 v[76:79], v176 offset:22528
	s_waitcnt vmcnt(6)
	s_waitcnt lgkmcnt(0)
	s_barrier
	s_setprio 1
	s_waitcnt lgkmcnt(0)
	v_mfma_f32_16x16x128_f8f6f4 v[44:47], v[178:185], v[48:55], 0
	v_mfma_f32_16x16x128_f8f6f4 v[36:39], v[186:193], v[48:55], 0
	v_mfma_f32_16x16x128_f8f6f4 v[28:31], v[178:185], v[56:63], 0
	v_mfma_f32_16x16x128_f8f6f4 v[24:27], v[186:193], v[56:63], 0
	v_mfma_f32_16x16x128_f8f6f4 v[20:23], v[178:185], v[64:71], 0
	v_mfma_f32_16x16x128_f8f6f4 v[16:19], v[186:193], v[64:71], 0
	v_mfma_f32_16x16x128_f8f6f4 v[12:15], v[178:185], v[72:79], 0
	v_mfma_f32_16x16x128_f8f6f4 v[8:11], v[186:193], v[72:79], 0
	s_setprio 0
	s_setprio 1
	v_mfma_f32_16x16x128_f8f6f4 v[4:7], v[194:201], v[48:55], 0
	v_mfma_f32_16x16x128_f8f6f4 v[0:3], v[202:209], v[48:55], 0
	v_mfma_f32_16x16x128_f8f6f4 v[104:107], v[194:201], v[56:63], 0
	v_mfma_f32_16x16x128_f8f6f4 v[108:111], v[202:209], v[56:63], 0
	v_mfma_f32_16x16x128_f8f6f4 v[112:115], v[194:201], v[64:71], 0
	v_mfma_f32_16x16x128_f8f6f4 v[116:119], v[202:209], v[64:71], 0
	v_mfma_f32_16x16x128_f8f6f4 v[120:123], v[194:201], v[72:79], 0
	v_mfma_f32_16x16x128_f8f6f4 v[124:127], v[202:209], v[72:79], 0
	s_setprio 0
	s_barrier
	s_add_i32 s64, 0, 0x18000
	s_add_i32 s65, 0, 0x1c000
	ds_read_b128 v[178:181], v168
	ds_read_b128 v[186:189], v168 offset:2048
	ds_read_b128 v[182:185], v169
	ds_read_b128 v[190:193], v169 offset:2048
	ds_read_b128 v[194:197], v170
	ds_read_b128 v[202:205], v170 offset:2048
	ds_read_b128 v[198:201], v171
	ds_read_b128 v[206:209], v171 offset:2048
	s_mov_b32 m0, s50
	v_mov_b32_e32 v128, v133
	ds_read_b128 v[48:51], v175 offset:32768
	ds_read_b128 v[210:213], v175 offset:34816
	ds_read_b128 v[52:55], v176 offset:32768
	ds_read_b128 v[214:217], v176 offset:34816
	ds_read_b128 v[218:221], v175 offset:36864
	ds_read_b128 v[226:229], v175 offset:38912
	ds_read_b128 v[222:225], v176 offset:36864
	ds_read_b128 v[230:233], v176 offset:38912
	s_mov_b32 m0, s1
	s_nop 0
	global_load_lds_dwordx4 v132, s[40:41]
	s_mov_b32 m0, s49
	s_nop 0
	global_load_lds_dwordx4 v134, s[40:41]
	s_mov_b32 m0, s50
	v_mov_b32_e32 v138, v131
	global_load_lds_dwordx4 v128, s[40:41]
	s_mov_b32 m0, s51
	s_nop 0
	global_load_lds_dwordx4 v138, s[40:41]
	s_waitcnt vmcnt(8)
	s_waitcnt lgkmcnt(0)
	s_barrier
	s_setprio 1
	s_waitcnt lgkmcnt(0)
	v_mfma_f32_16x16x128_f8f6f4 v[100:103], v[178:185], v[48:55], v[100:103]
	v_mfma_f32_16x16x128_f8f6f4 v[96:99], v[186:193], v[48:55], v[96:99]
	v_mfma_f32_16x16x128_f8f6f4 v[92:95], v[178:185], v[210:217], v[92:95]
	v_mfma_f32_16x16x128_f8f6f4 v[88:91], v[186:193], v[210:217], v[88:91]
	v_mfma_f32_16x16x128_f8f6f4 v[84:87], v[178:185], v[218:225], v[84:87]
	v_mfma_f32_16x16x128_f8f6f4 v[80:83], v[186:193], v[218:225], v[80:83]
	v_mfma_f32_16x16x128_f8f6f4 v[76:79], v[178:185], v[226:233], v[242:245]
	v_mfma_f32_16x16x128_f8f6f4 v[72:75], v[186:193], v[226:233], v[246:249]
	s_setprio 0
	s_setprio 1
	v_mfma_f32_16x16x128_f8f6f4 v[68:71], v[194:201], v[48:55], v[250:253]
	v_mfma_f32_16x16x128_f8f6f4 v[64:67], v[202:209], v[48:55], v[144:147]
	v_mfma_f32_16x16x128_f8f6f4 v[60:63], v[194:201], v[210:217], v[148:151]
	v_mfma_f32_16x16x128_f8f6f4 v[56:59], v[202:209], v[210:217], v[152:155]
	v_mfma_f32_16x16x128_f8f6f4 v[52:55], v[194:201], v[218:225], v[156:159]
	v_mfma_f32_16x16x128_f8f6f4 v[48:51], v[202:209], v[218:225], v[160:163]
	v_mfma_f32_16x16x128_f8f6f4 v[40:43], v[194:201], v[226:233], v[40:43]
	v_mfma_f32_16x16x128_f8f6f4 v[32:35], v[202:209], v[226:233], v[32:35]
	s_setprio 0
	s_barrier
	v_mov_b32_e32 v137, v129
	s_add_i32 s64, s64, s48
	s_add_u32 vcc_lo, s42, s14
	s_addc_u32 vcc_hi, s43, s15
	s_mov_b32 m0, s64
	v_mov_b32_e32 v131, v129
	global_load_lds_dwordx4 v136, vcc
	s_add_i32 m0, s64, 0x2000
	v_mov_b32_e32 v133, v129
	s_add_u32 s42, s42, 0x4080
	s_addc_u32 s43, s43, 0
	s_add_i32 s64, s65, s48
	global_load_lds_dwordx4 v130, vcc
	s_mov_b32 m0, s64
	v_mov_b32_e32 v135, v129
	global_load_lds_dwordx4 v136, s[42:43]
	s_add_i32 m0, s64, 0x2000
	s_nop 0
	global_load_lds_dwordx4 v130, s[42:43]
	s_mov_b32 m0, s53
	s_add_u32 vcc_lo, s40, s14
	s_addc_u32 vcc_hi, s41, s15
	global_load_lds_dwordx4 v132, vcc
	s_mov_b32 m0, s54
	s_nop 0
	global_load_lds_dwordx4 v134, vcc
	ds_read_b128 v[210:213], v175 offset:49152
	ds_read_b128 v[218:221], v175 offset:51200
	ds_read_b128 v[214:217], v176 offset:49152
	ds_read_b128 v[222:225], v176 offset:51200
	ds_read_b128 v[226:229], v175 offset:53248
	ds_read_b128 v[234:237], v175 offset:55296
	ds_read_b128 v[230:233], v176 offset:53248
	ds_read_b128 v[238:241], v176 offset:55296
	s_waitcnt vmcnt(8)
	s_waitcnt lgkmcnt(0)
	s_barrier
	s_setprio 1
	s_waitcnt lgkmcnt(0)
	v_mfma_f32_16x16x128_f8f6f4 v[44:47], v[178:185], v[210:217], v[44:47]
	v_mfma_f32_16x16x128_f8f6f4 v[36:39], v[186:193], v[210:217], v[36:39]
	v_mfma_f32_16x16x128_f8f6f4 v[28:31], v[178:185], v[218:225], v[28:31]
	v_mfma_f32_16x16x128_f8f6f4 v[24:27], v[186:193], v[218:225], v[24:27]
	v_mfma_f32_16x16x128_f8f6f4 v[20:23], v[178:185], v[226:233], v[20:23]
	v_mfma_f32_16x16x128_f8f6f4 v[16:19], v[186:193], v[226:233], v[16:19]
	v_mfma_f32_16x16x128_f8f6f4 v[12:15], v[178:185], v[234:241], v[12:15]
	v_mfma_f32_16x16x128_f8f6f4 v[8:11], v[186:193], v[234:241], v[8:11]
	s_setprio 0
	s_setprio 1
	v_mfma_f32_16x16x128_f8f6f4 v[4:7], v[194:201], v[210:217], v[4:7]
	v_mfma_f32_16x16x128_f8f6f4 v[0:3], v[202:209], v[210:217], v[0:3]
	v_mfma_f32_16x16x128_f8f6f4 v[104:107], v[194:201], v[218:225], v[104:107]
	v_mfma_f32_16x16x128_f8f6f4 v[108:111], v[202:209], v[218:225], v[108:111]
	v_mfma_f32_16x16x128_f8f6f4 v[112:115], v[194:201], v[226:233], v[112:115]
	v_mfma_f32_16x16x128_f8f6f4 v[116:119], v[202:209], v[226:233], v[116:119]
	v_mfma_f32_16x16x128_f8f6f4 v[120:123], v[194:201], v[234:241], v[120:123]
	v_mfma_f32_16x16x128_f8f6f4 v[124:127], v[202:209], v[234:241], v[124:127]
	s_setprio 0
	s_barrier
	s_add_i32 s45, s45, 2
	s_add_u32 s38, s38, 0x100
	s_addc_u32 s39, s39, 0
	s_branch .LBB0_1010
.LBB0_1009:
	s_add_u32 s64, s6, s38
	ds_read_b128 v[178:181], v164
	ds_read_b128 v[186:189], v164 offset:2048
	ds_read_b128 v[182:185], v165
	ds_read_b128 v[190:193], v165 offset:2048
	s_addc_u32 s65, s7, s39
	ds_read_b128 v[194:197], v166
	ds_read_b128 v[202:205], v166 offset:2048
	ds_read_b128 v[198:201], v167
	ds_read_b128 v[206:209], v167 offset:2048
	s_add_u32 s66, s64, 0x5e000100
	s_addc_u32 s67, s65, 0
	s_and_b64 s[40:41], s[42:43], exec
	s_cselect_b32 s41, s11, s67
	s_cselect_b32 s40, s10, s66
	s_add_u32 s66, s5, s38
	s_addc_u32 s67, s27, s39
	s_and_b64 s[42:43], s[42:43], exec
	s_cselect_b32 s43, s35, s67
	s_cselect_b32 s42, s34, s66
	ds_read_b128 v[210:213], v175
	ds_read_b128 v[218:221], v175 offset:2048
	ds_read_b128 v[214:217], v176
	ds_read_b128 v[222:225], v176 offset:2048
	ds_read_b128 v[226:229], v175 offset:4096
	ds_read_b128 v[234:237], v175 offset:6144
	ds_read_b128 v[230:233], v176 offset:4096
	ds_read_b128 v[238:241], v176 offset:6144
	s_add_i32 m0, s1, 0xc000
	s_add_u32 vcc_lo, s64, s16
	s_addc_u32 vcc_hi, s65, s17
	global_load_lds_dwordx4 v128, vcc
	v_mov_b32_e32 v139, v129
	s_add_i32 m0, s1, 0xe000
	s_nop 0
	global_load_lds_dwordx4 v138, vcc
	s_waitcnt vmcnt(8)
	s_waitcnt lgkmcnt(0)
	s_barrier
	s_setprio 1
	s_waitcnt lgkmcnt(0)
	v_mfma_f32_16x16x128_f8f6f4 v[100:103], v[178:185], v[210:217], v[100:103]
	v_mfma_f32_16x16x128_f8f6f4 v[96:99], v[186:193], v[210:217], v[96:99]
	v_mfma_f32_16x16x128_f8f6f4 v[92:95], v[178:185], v[218:225], v[92:95]
	v_mfma_f32_16x16x128_f8f6f4 v[88:91], v[186:193], v[218:225], v[88:91]
	v_mfma_f32_16x16x128_f8f6f4 v[84:87], v[178:185], v[226:233], v[84:87]
	v_mfma_f32_16x16x128_f8f6f4 v[80:83], v[186:193], v[226:233], v[80:83]
	v_mfma_f32_16x16x128_f8f6f4 v[242:245], v[178:185], v[234:241], v[76:79]
	v_mfma_f32_16x16x128_f8f6f4 v[246:249], v[186:193], v[234:241], v[72:75]
	s_setprio 0
	s_setprio 1
	v_mfma_f32_16x16x128_f8f6f4 v[40:43], v[194:201], v[234:241], v[40:43]
	v_mfma_f32_16x16x128_f8f6f4 v[32:35], v[202:209], v[234:241], v[32:35]
	v_mfma_f32_16x16x128_f8f6f4 v[250:253], v[194:201], v[210:217], v[68:71]
	v_mfma_f32_16x16x128_f8f6f4 v[144:147], v[202:209], v[210:217], v[64:67]
	v_mfma_f32_16x16x128_f8f6f4 v[148:151], v[194:201], v[218:225], v[60:63]
	v_mfma_f32_16x16x128_f8f6f4 v[152:155], v[202:209], v[218:225], v[56:59]
	v_mfma_f32_16x16x128_f8f6f4 v[156:159], v[194:201], v[226:233], v[52:55]
	v_mfma_f32_16x16x128_f8f6f4 v[160:163], v[202:209], v[226:233], v[48:51]
	s_setprio 0
	s_barrier
	s_add_i32 s64, s58, s48
	s_mov_b32 m0, s64
	s_nop 2
	s_nop 0
	global_load_lds_dwordx4 v136, s[42:43]
	s_add_i32 m0, s64, 0x2000
	s_add_u32 s64, s42, 0x4000
	s_addc_u32 s65, s43, 0
	s_add_i32 s66, s59, s48
	s_nop 0
	global_load_lds_dwordx4 v130, s[42:43]
	s_mov_b32 m0, s66
	s_nop 0
	global_load_lds_dwordx4 v136, s[64:65]
	s_add_i32 m0, s66, 0x2000
	s_nop 0
	global_load_lds_dwordx4 v130, s[64:65]
	ds_read_b128 v[48:51], v175 offset:16384
	ds_read_b128 v[56:59], v175 offset:18432
	ds_read_b128 v[52:55], v176 offset:16384
	ds_read_b128 v[60:63], v176 offset:18432
	ds_read_b128 v[64:67], v175 offset:20480
	ds_read_b128 v[72:75], v175 offset:22528
	ds_read_b128 v[68:71], v176 offset:20480
	ds_read_b128 v[76:79], v176 offset:22528
	s_waitcnt vmcnt(6)
	s_waitcnt lgkmcnt(0)
	s_barrier
	s_setprio 1
	s_waitcnt lgkmcnt(0)
	v_mfma_f32_16x16x128_f8f6f4 v[44:47], v[178:185], v[48:55], v[44:47]
	v_mfma_f32_16x16x128_f8f6f4 v[36:39], v[186:193], v[48:55], v[36:39]
	v_mfma_f32_16x16x128_f8f6f4 v[28:31], v[178:185], v[56:63], v[28:31]
	v_mfma_f32_16x16x128_f8f6f4 v[24:27], v[186:193], v[56:63], v[24:27]
	v_mfma_f32_16x16x128_f8f6f4 v[20:23], v[178:185], v[64:71], v[20:23]
	v_mfma_f32_16x16x128_f8f6f4 v[16:19], v[186:193], v[64:71], v[16:19]
	v_mfma_f32_16x16x128_f8f6f4 v[12:15], v[178:185], v[72:79], v[12:15]
	v_mfma_f32_16x16x128_f8f6f4 v[8:11], v[186:193], v[72:79], v[8:11]
	s_setprio 0
	s_setprio 1
	v_mfma_f32_16x16x128_f8f6f4 v[4:7], v[194:201], v[48:55], v[4:7]
	v_mfma_f32_16x16x128_f8f6f4 v[0:3], v[202:209], v[48:55], v[0:3]
	v_mfma_f32_16x16x128_f8f6f4 v[104:107], v[194:201], v[56:63], v[104:107]
	v_mfma_f32_16x16x128_f8f6f4 v[108:111], v[202:209], v[56:63], v[108:111]
	v_mfma_f32_16x16x128_f8f6f4 v[112:115], v[194:201], v[64:71], v[112:115]
	v_mfma_f32_16x16x128_f8f6f4 v[116:119], v[202:209], v[64:71], v[116:119]
	v_mfma_f32_16x16x128_f8f6f4 v[120:123], v[194:201], v[72:79], v[120:123]
	v_mfma_f32_16x16x128_f8f6f4 v[124:127], v[202:209], v[72:79], v[124:127]
	s_setprio 0
	s_barrier
	s_add_i32 s64, 0, 0x18000
	s_add_i32 s65, 0, 0x1c000
	ds_read_b128 v[178:181], v168
	ds_read_b128 v[186:189], v168 offset:2048
	ds_read_b128 v[182:185], v169
	ds_read_b128 v[190:193], v169 offset:2048
	ds_read_b128 v[194:197], v170
	ds_read_b128 v[202:205], v170 offset:2048
	ds_read_b128 v[198:201], v171
	ds_read_b128 v[206:209], v171 offset:2048
	s_mov_b32 m0, s50
	v_mov_b32_e32 v128, v133
	ds_read_b128 v[48:51], v175 offset:32768
	ds_read_b128 v[210:213], v175 offset:34816
	ds_read_b128 v[52:55], v176 offset:32768
	ds_read_b128 v[214:217], v176 offset:34816
	ds_read_b128 v[218:221], v175 offset:36864
	ds_read_b128 v[226:229], v175 offset:38912
	ds_read_b128 v[222:225], v176 offset:36864
	ds_read_b128 v[230:233], v176 offset:38912
	s_mov_b32 m0, s1
	s_nop 0
	global_load_lds_dwordx4 v132, s[40:41]
	s_mov_b32 m0, s49
	s_nop 0
	global_load_lds_dwordx4 v134, s[40:41]
	s_mov_b32 m0, s50
	v_mov_b32_e32 v138, v131
	global_load_lds_dwordx4 v128, s[40:41]
	s_mov_b32 m0, s51
	s_nop 0
	global_load_lds_dwordx4 v138, s[40:41]
	s_waitcnt vmcnt(8)
	s_waitcnt lgkmcnt(0)
	s_barrier
	s_setprio 1
	s_waitcnt lgkmcnt(0)
	v_mfma_f32_16x16x128_f8f6f4 v[100:103], v[178:185], v[48:55], v[100:103]
	v_mfma_f32_16x16x128_f8f6f4 v[96:99], v[186:193], v[48:55], v[96:99]
	v_mfma_f32_16x16x128_f8f6f4 v[92:95], v[178:185], v[210:217], v[92:95]
	v_mfma_f32_16x16x128_f8f6f4 v[88:91], v[186:193], v[210:217], v[88:91]
	v_mfma_f32_16x16x128_f8f6f4 v[84:87], v[178:185], v[218:225], v[84:87]
	v_mfma_f32_16x16x128_f8f6f4 v[80:83], v[186:193], v[218:225], v[80:83]
	v_mfma_f32_16x16x128_f8f6f4 v[76:79], v[178:185], v[226:233], v[242:245]
	v_mfma_f32_16x16x128_f8f6f4 v[72:75], v[186:193], v[226:233], v[246:249]
	s_setprio 0
	s_setprio 1
	v_mfma_f32_16x16x128_f8f6f4 v[68:71], v[194:201], v[48:55], v[250:253]
	v_mfma_f32_16x16x128_f8f6f4 v[64:67], v[202:209], v[48:55], v[144:147]
	v_mfma_f32_16x16x128_f8f6f4 v[60:63], v[194:201], v[210:217], v[148:151]
	v_mfma_f32_16x16x128_f8f6f4 v[56:59], v[202:209], v[210:217], v[152:155]
	v_mfma_f32_16x16x128_f8f6f4 v[52:55], v[194:201], v[218:225], v[156:159]
	v_mfma_f32_16x16x128_f8f6f4 v[48:51], v[202:209], v[218:225], v[160:163]
	v_mfma_f32_16x16x128_f8f6f4 v[40:43], v[194:201], v[226:233], v[40:43]
	v_mfma_f32_16x16x128_f8f6f4 v[32:35], v[202:209], v[226:233], v[32:35]
	s_setprio 0
	s_barrier
	v_mov_b32_e32 v137, v129
	s_add_i32 s64, s64, s48
	s_add_u32 vcc_lo, s42, s14
	s_addc_u32 vcc_hi, s43, s15
	s_mov_b32 m0, s64
	v_mov_b32_e32 v131, v129
	global_load_lds_dwordx4 v136, vcc
	s_add_i32 m0, s64, 0x2000
	v_mov_b32_e32 v133, v129
	s_add_u32 s42, s42, 0x4080
	s_addc_u32 s43, s43, 0
	s_add_i32 s64, s65, s48
	global_load_lds_dwordx4 v130, vcc
	s_mov_b32 m0, s64
	v_mov_b32_e32 v135, v129
	global_load_lds_dwordx4 v136, s[42:43]
	s_add_i32 m0, s64, 0x2000
	s_nop 0
	global_load_lds_dwordx4 v130, s[42:43]
	s_mov_b32 m0, s53
	s_add_u32 vcc_lo, s40, s14
	s_addc_u32 vcc_hi, s41, s15
	global_load_lds_dwordx4 v132, vcc
	s_mov_b32 m0, s54
	s_nop 0
	global_load_lds_dwordx4 v134, vcc
	ds_read_b128 v[210:213], v175 offset:49152
	ds_read_b128 v[218:221], v175 offset:51200
	ds_read_b128 v[214:217], v176 offset:49152
	ds_read_b128 v[222:225], v176 offset:51200
	ds_read_b128 v[226:229], v175 offset:53248
	ds_read_b128 v[234:237], v175 offset:55296
	ds_read_b128 v[230:233], v176 offset:53248
	ds_read_b128 v[238:241], v176 offset:55296
	s_waitcnt vmcnt(8)
	s_waitcnt lgkmcnt(0)
	s_barrier
	s_setprio 1
	s_waitcnt lgkmcnt(0)
	v_mfma_f32_16x16x128_f8f6f4 v[44:47], v[178:185], v[210:217], v[44:47]
	v_mfma_f32_16x16x128_f8f6f4 v[36:39], v[186:193], v[210:217], v[36:39]
	v_mfma_f32_16x16x128_f8f6f4 v[28:31], v[178:185], v[218:225], v[28:31]
	v_mfma_f32_16x16x128_f8f6f4 v[24:27], v[186:193], v[218:225], v[24:27]
	v_mfma_f32_16x16x128_f8f6f4 v[20:23], v[178:185], v[226:233], v[20:23]
	v_mfma_f32_16x16x128_f8f6f4 v[16:19], v[186:193], v[226:233], v[16:19]
	v_mfma_f32_16x16x128_f8f6f4 v[12:15], v[178:185], v[234:241], v[12:15]
	v_mfma_f32_16x16x128_f8f6f4 v[8:11], v[186:193], v[234:241], v[8:11]
	s_setprio 0
	s_setprio 1
	v_mfma_f32_16x16x128_f8f6f4 v[4:7], v[194:201], v[210:217], v[4:7]
	v_mfma_f32_16x16x128_f8f6f4 v[0:3], v[202:209], v[210:217], v[0:3]
	v_mfma_f32_16x16x128_f8f6f4 v[104:107], v[194:201], v[218:225], v[104:107]
	v_mfma_f32_16x16x128_f8f6f4 v[108:111], v[202:209], v[218:225], v[108:111]
	v_mfma_f32_16x16x128_f8f6f4 v[112:115], v[194:201], v[226:233], v[112:115]
	v_mfma_f32_16x16x128_f8f6f4 v[116:119], v[202:209], v[226:233], v[116:119]
	v_mfma_f32_16x16x128_f8f6f4 v[120:123], v[194:201], v[234:241], v[120:123]
	v_mfma_f32_16x16x128_f8f6f4 v[124:127], v[202:209], v[234:241], v[124:127]
	s_setprio 0
	s_barrier
	s_add_i32 s45, s45, 2
	s_add_u32 s38, s38, 0x100
	s_addc_u32 s39, s39, 0
	s_cmp_gt_u32 s45, 13
	s_cbranch_scc1 .LBB0_1012
